# MLA QK: K-fragment LDS reads issued two steps ahead (plus PTK prefetch, RTO/rtp batching)
# speedup vs baseline: 1.0043x; 1.0002x over previous
.LBB0_656:
	v_lshl_add_u64 v[64:65], s[12:13], 0, v[96:97]
	v_lshl_add_u64 v[66:67], v[64:65], 0, v[172:173]
	v_lshl_add_u64 v[64:65], v[64:65], 0, v[174:175]
	global_load_dwordx4 v[162:165], v[66:67], off
	global_load_dwordx4 v[158:161], v[64:65], off
	v_lshl_add_u64 v[64:65], s[6:7], 0, v[182:183]
	v_lshl_add_u64 v[64:65], v[176:177], 1, v[64:65]
	v_lshl_add_u64 v[66:67], s[6:7], 0, v[184:185]
	v_lshl_add_u64 v[66:67], v[178:179], 1, v[66:67]
	global_load_dwordx4 v[150:153], v[64:65], off
	global_load_dwordx4 v[146:149], v[66:67], off
	v_lshl_add_u64 v[64:65], s[6:7], 0, v[186:187]
	v_lshl_add_u64 v[64:65], v[180:181], 1, v[64:65]
	global_load_dwordx4 v[154:157], v[64:65], off
	s_and_b32 s24, s24, 1
	s_mul_i32 s6, s24, 0x6000
	s_add_i32 s6, s6, 0
	v_add_u32_e32 v166, s6, v234
	v_add3_u32 v167, s6, v235, v234
	ds_read_b128 v[64:67], v167 offset:32768
	v_add_u32_e32 v167, v166, v235
	ds_read_b128 v[68:71], v167 offset:45056
	v_add3_u32 v167, s6, v232, v234
	ds_read_b128 v[208:211], v167 offset:32768
	v_add_u32_e32 v167, v166, v232
	ds_read_b128 v[214:217], v167 offset:45056
	v_add3_u32 v167, s6, v228, v234
	ds_read_b128 v[244:247], v167 offset:32768
	v_add_u32_e32 v167, v166, v228
	ds_read_b128 v[248:251], v167 offset:45056
	s_waitcnt lgkmcnt(5)
	v_mfma_f32_32x32x16_bf16 v[80:95], v[64:67], v[102:105], 0
	s_waitcnt lgkmcnt(4)
	v_mfma_f32_32x32x16_bf16 v[64:79], v[68:71], v[102:105], 0
	s_waitcnt lgkmcnt(3)
	v_mfma_f32_32x32x16_bf16 v[80:95], v[208:211], v[98:101], v[80:95]
	v_add3_u32 v167, s6, v206, v234
	ds_read_b128 v[208:211], v167 offset:32768
	s_waitcnt lgkmcnt(3)
	v_mfma_f32_32x32x16_bf16 v[64:79], v[214:217], v[98:101], v[64:79]
	v_add_u32_e32 v167, v166, v206
	ds_read_b128 v[214:217], v167 offset:45056
	s_waitcnt vmcnt(14)
	s_waitcnt lgkmcnt(3)
	v_mfma_f32_32x32x16_bf16 v[80:95], v[244:247], v[142:145], v[80:95]
	v_add3_u32 v167, s6, v203, v234
	ds_read_b128 v[244:247], v167 offset:32768
	s_waitcnt lgkmcnt(3)
	v_mfma_f32_32x32x16_bf16 v[64:79], v[248:251], v[142:145], v[64:79]
	v_add_u32_e32 v167, v166, v203
	ds_read_b128 v[248:251], v167 offset:45056
	s_waitcnt vmcnt(13)
	s_waitcnt lgkmcnt(3)
	v_mfma_f32_32x32x16_bf16 v[80:95], v[208:211], v[138:141], v[80:95]
	v_add3_u32 v167, s6, v201, v234
	ds_read_b128 v[208:211], v167 offset:32768
	s_waitcnt lgkmcnt(3)
	v_mfma_f32_32x32x16_bf16 v[64:79], v[214:217], v[138:141], v[64:79]
	v_add_u32_e32 v167, v166, v201
	ds_read_b128 v[214:217], v167 offset:45056
	s_waitcnt vmcnt(12)
	s_waitcnt lgkmcnt(3)
	v_mfma_f32_32x32x16_bf16 v[80:95], v[244:247], v[134:137], v[80:95]
	v_add3_u32 v167, s6, v199, v234
	ds_read_b128 v[244:247], v167 offset:32768
	s_waitcnt lgkmcnt(3)
	v_mfma_f32_32x32x16_bf16 v[64:79], v[248:251], v[134:137], v[64:79]
	v_add_u32_e32 v167, v166, v199
	ds_read_b128 v[248:251], v167 offset:45056
	s_waitcnt vmcnt(11)
	s_waitcnt lgkmcnt(3)
	v_mfma_f32_32x32x16_bf16 v[80:95], v[208:211], v[130:133], v[80:95]
	v_add3_u32 v167, s6, v196, v234
	ds_read_b128 v[208:211], v167 offset:32768
	s_waitcnt lgkmcnt(3)
	v_mfma_f32_32x32x16_bf16 v[64:79], v[214:217], v[130:133], v[64:79]
	v_add_u32_e32 v167, v166, v196
	ds_read_b128 v[214:217], v167 offset:45056
	s_waitcnt vmcnt(10)
	s_waitcnt lgkmcnt(3)
	v_mfma_f32_32x32x16_bf16 v[80:95], v[244:247], v[126:129], v[80:95]
	v_add3_u32 v167, s6, v195, v234
	ds_read_b128 v[244:247], v167 offset:32768
	s_waitcnt lgkmcnt(3)
	v_mfma_f32_32x32x16_bf16 v[64:79], v[248:251], v[126:129], v[64:79]
	v_add_u32_e32 v167, v166, v195
	ds_read_b128 v[248:251], v167 offset:45056
	s_waitcnt vmcnt(9)
	s_waitcnt lgkmcnt(3)
	v_mfma_f32_32x32x16_bf16 v[80:95], v[208:211], v[122:125], v[80:95]
	v_add3_u32 v167, s6, v194, v234
	ds_read_b128 v[208:211], v167 offset:32768
	s_waitcnt lgkmcnt(3)
	v_mfma_f32_32x32x16_bf16 v[64:79], v[214:217], v[122:125], v[64:79]
	v_add_u32_e32 v167, v166, v194
	ds_read_b128 v[214:217], v167 offset:45056
	s_waitcnt vmcnt(8)
	s_waitcnt lgkmcnt(3)
	v_mfma_f32_32x32x16_bf16 v[80:95], v[244:247], v[118:121], v[80:95]
	v_add3_u32 v167, s6, v193, v234
	ds_read_b128 v[244:247], v167 offset:32768
	s_waitcnt lgkmcnt(3)
	v_mfma_f32_32x32x16_bf16 v[64:79], v[248:251], v[118:121], v[64:79]
	v_add_u32_e32 v167, v166, v193
	ds_read_b128 v[248:251], v167 offset:45056
	s_waitcnt vmcnt(7)
	s_waitcnt lgkmcnt(3)
	v_mfma_f32_32x32x16_bf16 v[80:95], v[208:211], v[114:117], v[80:95]
	v_add3_u32 v167, s6, v192, v234
	ds_read_b128 v[208:211], v167 offset:32768
	s_waitcnt lgkmcnt(3)
	v_mfma_f32_32x32x16_bf16 v[64:79], v[214:217], v[114:117], v[64:79]
	v_add_u32_e32 v167, v166, v192
	ds_read_b128 v[214:217], v167 offset:45056
	s_waitcnt vmcnt(6)
	s_waitcnt lgkmcnt(3)
	v_mfma_f32_32x32x16_bf16 v[80:95], v[244:247], v[110:113], v[80:95]
	s_waitcnt lgkmcnt(2)
	v_mfma_f32_32x32x16_bf16 v[64:79], v[248:251], v[110:113], v[64:79]
	s_waitcnt vmcnt(5)
	s_waitcnt lgkmcnt(1)
	v_mfma_f32_32x32x16_bf16 v[80:95], v[208:211], v[106:109], v[80:95]
	s_waitcnt lgkmcnt(0)
	v_mfma_f32_32x32x16_bf16 v[64:79], v[214:217], v[106:109], v[64:79]
	s_mov_b32 s6, 0x42ddb3d8
	s_nop 9
	v_max_f32_e32 v166, v81, v81
	v_max_f32_e32 v167, v80, v80
	v_max_f32_e32 v166, v167, v166
	v_max3_f32 v166, v166, v82, v83
	v_max3_f32 v166, v166, v84, v85
	v_max3_f32 v166, v166, v86, v87
	v_max3_f32 v166, v166, v88, v89
	v_max3_f32 v166, v166, v90, v91
	v_max3_f32 v166, v166, v92, v93
	v_max3_f32 v166, v166, v94, v95
	v_max3_f32 v166, v166, v64, v65
	v_max3_f32 v166, v166, v66, v67
	v_max3_f32 v166, v166, v68, v69
	v_max3_f32 v166, v166, v70, v71
	v_max3_f32 v166, v166, v72, v73
	v_max3_f32 v166, v166, v74, v75
	v_max3_f32 v166, v166, v76, v77
	v_max3_f32 v166, v166, v78, v79
	v_mov_b32_e32 v167, v166
	s_nop 1
	v_permlane32_swap_b32_e32 v166, v167
	v_max_f32_e32 v167, v167, v167
	v_max_f32_e32 v166, v166, v166
	v_max_f32_e32 v166, v166, v167
	v_sub_f32_e32 v167, v166, v191
	v_cmp_ge_f32_e32 vcc, s6, v167
	v_max_f32_e32 v167, v191, v191
	v_max_f32_e32 v197, v167, v166
	v_sub_f32_e32 v166, v191, v197
	v_mul_f32_e32 v166, 0x3dd53b94, v166
	v_exp_f32_e32 v166, v166
	s_cmp_eq_u64 vcc, exec
	s_cselect_b64 s[6:7], -1, 0
	v_cndmask_b32_e64 v237, v166, 1.0, s[6:7]
	v_cmp_gt_f32_e32 vcc, 1.0, v237
	s_cbranch_vccz .LBB0_660
	s_and_saveexec_b64 s[12:13], s[4:5]
	ds_write_b32 v169, v237 offset:128
	s_or_b64 exec, exec, s[12:13]
	s_waitcnt lgkmcnt(0)
	v_add_u32_e32 v166, v171, v170
	ds_read_b128 v[208:211], v166 offset:224
	ds_read_b128 v[214:217], v166 offset:192
	ds_read_b128 v[220:223], v166 offset:160
	ds_read_b128 v[238:241], v166 offset:128
	s_waitcnt lgkmcnt(3)
	v_pk_mul_f32 v[60:61], v[60:61], v[208:209]
	s_waitcnt lgkmcnt(2)
	v_pk_mul_f32 v[56:57], v[56:57], v[214:215]
	s_waitcnt lgkmcnt(1)
	v_pk_mul_f32 v[52:53], v[52:53], v[220:221]
	v_pk_mul_f32 v[62:63], v[62:63], v[210:211]
	v_pk_mul_f32 v[58:59], v[58:59], v[216:217]
	v_pk_mul_f32 v[54:55], v[54:55], v[222:223]
	s_waitcnt lgkmcnt(0)
	v_pk_mul_f32 v[50:51], v[50:51], v[240:241]
	v_pk_mul_f32 v[48:49], v[48:49], v[238:239]
	v_pk_mul_f32 v[44:45], v[44:45], v[208:209]
	v_pk_mul_f32 v[40:41], v[40:41], v[214:215]
	v_pk_mul_f32 v[36:37], v[36:37], v[220:221]
	v_pk_mul_f32 v[46:47], v[46:47], v[210:211]
	v_pk_mul_f32 v[42:43], v[42:43], v[216:217]
	v_pk_mul_f32 v[38:39], v[38:39], v[222:223]
	v_pk_mul_f32 v[34:35], v[34:35], v[240:241]
	v_pk_mul_f32 v[32:33], v[32:33], v[238:239]
	v_pk_mul_f32 v[28:29], v[28:29], v[208:209]
	v_pk_mul_f32 v[24:25], v[24:25], v[214:215]
	v_pk_mul_f32 v[20:21], v[20:21], v[220:221]
	v_pk_mul_f32 v[30:31], v[30:31], v[210:211]
	v_pk_mul_f32 v[26:27], v[26:27], v[216:217]
	v_pk_mul_f32 v[22:23], v[22:23], v[222:223]
	v_pk_mul_f32 v[18:19], v[18:19], v[240:241]
	v_pk_mul_f32 v[16:17], v[16:17], v[238:239]
	v_pk_mul_f32 v[12:13], v[12:13], v[208:209]
	v_pk_mul_f32 v[8:9], v[8:9], v[214:215]
	v_pk_mul_f32 v[4:5], v[4:5], v[220:221]
	v_pk_mul_f32 v[14:15], v[14:15], v[210:211]
	v_pk_mul_f32 v[10:11], v[10:11], v[216:217]
	v_pk_mul_f32 v[6:7], v[6:7], v[222:223]
	v_pk_mul_f32 v[2:3], v[2:3], v[240:241]
	v_pk_mul_f32 v[0:1], v[0:1], v[238:239]
